# fp8 GEMM loops: first K iteration peeled with SrcC=0 MFMAs, per-unit accumulator zeroing removed
# speedup vs baseline: 1.0100x; 1.0053x over previous
.LBB0_459:
	s_and_b64 s[46:47], s[38:39], exec
	s_cselect_b32 s48, s35, s43
	s_cselect_b32 s49, s34, s42
	s_cselect_b32 s66, s37, s45
	s_cselect_b32 s67, s36, s44
	s_add_u32 s42, s42, 0x80
	s_addc_u32 s43, s43, 0
	s_add_u32 s68, s44, 0x100
	s_addc_u32 s69, s45, 0
	s_mov_b32 s70, -2
	ds_read_b128 v[18:21], v194
	ds_read_b128 v[22:25], v194 offset:1024
	ds_read_b128 v[26:29], v194 offset:2048
	ds_read_b128 v[30:33], v194 offset:3072
	ds_read_b128 v[2:5], v195
	ds_read_b128 v[6:9], v195 offset:1024
	ds_read_b128 v[10:13], v195 offset:2048
	ds_read_b128 v[14:17], v195 offset:3072
	s_add_u32 s44, s42, 0x80
	s_addc_u32 s45, s43, 0
	s_cmp_eq_u32 s70, 12
	s_cselect_b32 s47, s48, s45
	s_cselect_b32 s46, s49, s44
	s_cselect_b32 s45, s66, s69
	s_cselect_b32 s44, s67, s68
	v_lshl_add_u64 v[222:223], s[42:43], 0, v[180:181]
	s_add_i32 m0, s41, 0xc000
	ds_read_b128 v[184:187], v196
	ds_read_b128 v[188:191], v196 offset:1024
	ds_read_b128 v[198:201], v196 offset:2048
	ds_read_b128 v[202:205], v196 offset:3072
	ds_read_b128 v[206:209], v196 offset:4096
	ds_read_b128 v[210:213], v196 offset:5120
	ds_read_b128 v[214:217], v196 offset:6144
	ds_read_b128 v[218:221], v196 offset:7168
	global_load_lds_dwordx4 v[222:223], off
	v_lshl_add_u64 v[222:223], s[42:43], 0, v[178:179]
	s_add_i32 m0, s41, 0xe000
	s_nop 0
	global_load_lds_dwordx4 v[222:223], off
	s_waitcnt vmcnt(8)
	s_waitcnt lgkmcnt(0)
	s_barrier
	s_setprio 1
	s_waitcnt lgkmcnt(0)
	s_nop 1
	v_mfma_f32_16x16x128_f8f6f4 v[158:161], v[18:25], v[184:191], 0
	v_mfma_f32_16x16x128_f8f6f4 v[154:157], v[26:33], v[184:191], 0
	v_mfma_f32_16x16x128_f8f6f4 v[142:145], v[18:25], v[198:205], 0
	v_mfma_f32_16x16x128_f8f6f4 v[138:141], v[26:33], v[198:205], 0
	v_mfma_f32_16x16x128_f8f6f4 v[126:129], v[18:25], v[206:213], 0
	v_mfma_f32_16x16x128_f8f6f4 v[122:125], v[26:33], v[206:213], 0
	v_mfma_f32_16x16x128_f8f6f4 v[110:113], v[18:25], v[214:221], 0
	v_mfma_f32_16x16x128_f8f6f4 v[106:109], v[26:33], v[214:221], 0
	s_setprio 0
	s_setprio 1
	s_nop 1
	v_mfma_f32_16x16x128_f8f6f4 v[150:153], v[2:9], v[184:191], 0
	v_mfma_f32_16x16x128_f8f6f4 v[146:149], v[10:17], v[184:191], 0
	v_mfma_f32_16x16x128_f8f6f4 v[134:137], v[2:9], v[198:205], 0
	v_mfma_f32_16x16x128_f8f6f4 v[130:133], v[10:17], v[198:205], 0
	v_mfma_f32_16x16x128_f8f6f4 v[118:121], v[2:9], v[206:213], 0
	v_mfma_f32_16x16x128_f8f6f4 v[114:117], v[10:17], v[206:213], 0
	v_mfma_f32_16x16x128_f8f6f4 v[102:105], v[2:9], v[214:221], 0
	v_mfma_f32_16x16x128_f8f6f4 v[98:101], v[10:17], v[214:221], 0
	s_setprio 0
	s_barrier
	s_add_i32 s71, s61, s53
	v_lshl_add_u64 v[184:185], s[44:45], 0, v[162:163]
	s_mov_b32 m0, s71
	ds_read_b128 v[198:201], v196 offset:16384
	ds_read_b128 v[202:205], v196 offset:17408
	ds_read_b128 v[206:209], v196 offset:18432
	ds_read_b128 v[210:213], v196 offset:19456
	ds_read_b128 v[214:217], v196 offset:20480
	ds_read_b128 v[218:221], v196 offset:21504
	ds_read_b128 v[230:233], v196 offset:22528
	ds_read_b128 v[234:237], v196 offset:23552
	global_load_lds_dwordx4 v[184:185], off
	s_add_i32 m0, s71, 0x2000
	s_add_u32 s72, s44, 0x40000
	v_lshl_add_u64 v[186:187], s[44:45], 0, v[164:165]
	s_addc_u32 s73, s45, 0
	s_add_i32 s71, s62, s53
	global_load_lds_dwordx4 v[186:187], off
	v_lshl_add_u64 v[188:189], s[72:73], 0, v[162:163]
	s_mov_b32 m0, s71
	v_lshl_add_u64 v[190:191], s[46:47], 0, v[168:169]
	global_load_lds_dwordx4 v[188:189], off
	v_lshl_add_u64 v[188:189], s[72:73], 0, v[164:165]
	s_add_i32 m0, s71, 0x2000
	s_nop 0
	global_load_lds_dwordx4 v[188:189], off
	v_lshl_add_u64 v[188:189], s[46:47], 0, v[166:167]
	s_mov_b32 m0, s41
	s_nop 0
	global_load_lds_dwordx4 v[188:189], off
	s_mov_b32 m0, s54
	s_nop 0
	global_load_lds_dwordx4 v[190:191], off
	s_waitcnt vmcnt(8)
	s_waitcnt lgkmcnt(0)
	s_barrier
	s_setprio 1
	s_waitcnt lgkmcnt(0)
	s_nop 1
	v_mfma_f32_16x16x128_f8f6f4 v[90:93], v[18:25], v[198:205], 0
	v_mfma_f32_16x16x128_f8f6f4 v[82:85], v[26:33], v[198:205], 0
	v_mfma_f32_16x16x128_f8f6f4 v[70:73], v[18:25], v[206:213], 0
	v_mfma_f32_16x16x128_f8f6f4 v[66:69], v[26:33], v[206:213], 0
	v_mfma_f32_16x16x128_f8f6f4 v[54:57], v[18:25], v[214:221], 0
	v_mfma_f32_16x16x128_f8f6f4 v[50:53], v[26:33], v[214:221], 0
	v_mfma_f32_16x16x128_f8f6f4 v[38:41], v[18:25], v[230:237], 0
	v_mfma_f32_16x16x128_f8f6f4 v[34:37], v[26:33], v[230:237], 0
	s_setprio 0
	s_setprio 1
	s_nop 1
	v_mfma_f32_16x16x128_f8f6f4 v[94:97], v[2:9], v[198:205], 0
	v_mfma_f32_16x16x128_f8f6f4 v[86:89], v[10:17], v[198:205], 0
	v_mfma_f32_16x16x128_f8f6f4 v[78:81], v[2:9], v[206:213], 0
	v_mfma_f32_16x16x128_f8f6f4 v[74:77], v[10:17], v[206:213], 0
	v_mfma_f32_16x16x128_f8f6f4 v[62:65], v[2:9], v[214:221], 0
	v_mfma_f32_16x16x128_f8f6f4 v[58:61], v[10:17], v[214:221], 0
	v_mfma_f32_16x16x128_f8f6f4 v[46:49], v[2:9], v[230:237], 0
	v_mfma_f32_16x16x128_f8f6f4 v[42:45], v[10:17], v[230:237], 0
	s_setprio 0
	s_barrier
	s_add_i32 s71, 0, 0x18000
	s_add_i32 s72, 0, 0x1c000
	v_add_u32_e32 v14, s71, v192
	v_add_u32_e32 v30, s72, v192
	ds_read_b128 v[2:5], v14
	ds_read_b128 v[6:9], v14 offset:1024
	ds_read_b128 v[10:13], v14 offset:2048
	ds_read_b128 v[14:17], v14 offset:3072
	ds_read_b128 v[18:21], v30
	ds_read_b128 v[22:25], v30 offset:1024
	ds_read_b128 v[26:29], v30 offset:2048
	ds_read_b128 v[30:33], v30 offset:3072
	s_mov_b32 m0, s55
	v_lshl_add_u64 v[222:223], s[46:47], 0, v[170:171]
	ds_read_b128 v[198:201], v196 offset:32768
	ds_read_b128 v[202:205], v196 offset:33792
	ds_read_b128 v[206:209], v196 offset:34816
	ds_read_b128 v[210:213], v196 offset:35840
	ds_read_b128 v[214:217], v196 offset:36864
	ds_read_b128 v[218:221], v196 offset:37888
	ds_read_b128 v[230:233], v196 offset:38912
	ds_read_b128 v[234:237], v196 offset:39936
	global_load_lds_dwordx4 v[222:223], off
	v_lshl_add_u64 v[222:223], s[46:47], 0, v[172:173]
	s_mov_b32 m0, s58
	s_nop 0
	global_load_lds_dwordx4 v[222:223], off
	s_waitcnt vmcnt(8)
	s_waitcnt lgkmcnt(0)
	s_barrier
	s_setprio 1
	s_waitcnt lgkmcnt(0)
	s_nop 1
	v_mfma_f32_16x16x128_f8f6f4 v[158:161], v[2:9], v[198:205], v[158:161]
	v_mfma_f32_16x16x128_f8f6f4 v[154:157], v[10:17], v[198:205], v[154:157]
	v_mfma_f32_16x16x128_f8f6f4 v[142:145], v[2:9], v[206:213], v[142:145]
	v_mfma_f32_16x16x128_f8f6f4 v[138:141], v[10:17], v[206:213], v[138:141]
	v_mfma_f32_16x16x128_f8f6f4 v[126:129], v[2:9], v[214:221], v[126:129]
	v_mfma_f32_16x16x128_f8f6f4 v[122:125], v[10:17], v[214:221], v[122:125]
	v_mfma_f32_16x16x128_f8f6f4 v[110:113], v[2:9], v[230:237], v[110:113]
	v_mfma_f32_16x16x128_f8f6f4 v[106:109], v[10:17], v[230:237], v[106:109]
	s_setprio 0
	s_setprio 1
	s_nop 1
	v_mfma_f32_16x16x128_f8f6f4 v[150:153], v[18:25], v[198:205], v[150:153]
	v_mfma_f32_16x16x128_f8f6f4 v[146:149], v[26:33], v[198:205], v[146:149]
	v_mfma_f32_16x16x128_f8f6f4 v[134:137], v[18:25], v[206:213], v[134:137]
	v_mfma_f32_16x16x128_f8f6f4 v[130:133], v[26:33], v[206:213], v[130:133]
	v_mfma_f32_16x16x128_f8f6f4 v[118:121], v[18:25], v[214:221], v[118:121]
	v_mfma_f32_16x16x128_f8f6f4 v[114:117], v[26:33], v[214:221], v[114:117]
	v_mfma_f32_16x16x128_f8f6f4 v[102:105], v[18:25], v[230:237], v[102:105]
	v_mfma_f32_16x16x128_f8f6f4 v[98:101], v[26:33], v[230:237], v[98:101]
	s_setprio 0
	s_barrier
	s_add_i32 s46, s71, s53
	v_lshl_add_u64 v[184:185], v[184:185], 0, s[12:13]
	s_mov_b32 m0, s46
	ds_read_b128 v[198:201], v196 offset:49152
	ds_read_b128 v[202:205], v196 offset:50176
	ds_read_b128 v[206:209], v196 offset:51200
	ds_read_b128 v[210:213], v196 offset:52224
	ds_read_b128 v[214:217], v196 offset:53248
	ds_read_b128 v[218:221], v196 offset:54272
	ds_read_b128 v[230:233], v196 offset:55296
	ds_read_b128 v[234:237], v196 offset:56320
	global_load_lds_dwordx4 v[184:185], off
	s_add_i32 m0, s46, 0x2000
	s_add_u32 s44, s44, 0x40080
	v_lshl_add_u64 v[184:185], v[186:187], 0, s[12:13]
	s_addc_u32 s45, s45, 0
	s_add_i32 s46, s72, s53
	global_load_lds_dwordx4 v[184:185], off
	v_lshl_add_u64 v[184:185], s[44:45], 0, v[162:163]
	s_mov_b32 m0, s46
	s_nop 0
	global_load_lds_dwordx4 v[184:185], off
	v_lshl_add_u64 v[184:185], s[44:45], 0, v[164:165]
	s_add_i32 m0, s46, 0x2000
	s_nop 0
	global_load_lds_dwordx4 v[184:185], off
	v_lshl_add_u64 v[184:185], v[188:189], 0, s[12:13]
	s_mov_b32 m0, s59
	s_nop 0
	global_load_lds_dwordx4 v[184:185], off
	v_lshl_add_u64 v[184:185], v[190:191], 0, s[12:13]
	s_mov_b32 m0, s60
	s_nop 0
	global_load_lds_dwordx4 v[184:185], off
	s_waitcnt vmcnt(8)
	s_waitcnt lgkmcnt(0)
	s_barrier
	s_setprio 1
	s_waitcnt lgkmcnt(0)
	s_nop 1
	v_mfma_f32_16x16x128_f8f6f4 v[90:93], v[2:9], v[198:205], v[90:93]
	v_mfma_f32_16x16x128_f8f6f4 v[82:85], v[10:17], v[198:205], v[82:85]
	v_mfma_f32_16x16x128_f8f6f4 v[70:73], v[2:9], v[206:213], v[70:73]
	v_mfma_f32_16x16x128_f8f6f4 v[66:69], v[10:17], v[206:213], v[66:69]
	v_mfma_f32_16x16x128_f8f6f4 v[54:57], v[2:9], v[214:221], v[54:57]
	v_mfma_f32_16x16x128_f8f6f4 v[50:53], v[10:17], v[214:221], v[50:53]
	v_mfma_f32_16x16x128_f8f6f4 v[38:41], v[2:9], v[230:237], v[38:41]
	v_mfma_f32_16x16x128_f8f6f4 v[34:37], v[10:17], v[230:237], v[34:37]
	s_setprio 0
	s_setprio 1
	s_nop 1
	v_mfma_f32_16x16x128_f8f6f4 v[94:97], v[18:25], v[198:205], v[94:97]
	v_mfma_f32_16x16x128_f8f6f4 v[86:89], v[26:33], v[198:205], v[86:89]
	v_mfma_f32_16x16x128_f8f6f4 v[78:81], v[18:25], v[206:213], v[78:81]
	v_mfma_f32_16x16x128_f8f6f4 v[74:77], v[26:33], v[206:213], v[74:77]
	v_mfma_f32_16x16x128_f8f6f4 v[62:65], v[18:25], v[214:221], v[62:65]
	v_mfma_f32_16x16x128_f8f6f4 v[58:61], v[26:33], v[214:221], v[58:61]
	v_mfma_f32_16x16x128_f8f6f4 v[46:49], v[18:25], v[230:237], v[46:49]
	v_mfma_f32_16x16x128_f8f6f4 v[42:45], v[26:33], v[230:237], v[42:45]
	s_setprio 0
	s_barrier
	s_add_i32 s70, s70, 2
	s_add_u32 s42, s42, 0x100
	s_addc_u32 s43, s43, 0
	s_add_u32 s68, s68, 0x100
	s_addc_u32 s69, s69, 0
	s_cmp_gt_u32 s70, 13
	s_cbranch_scc0 .LBB0_460
	s_branch .Lmy_pexit_p1b

.Lmy_pexit_p1b:
	s_and_b64 vcc, exec, s[0:1]
	s_cbranch_vccz .LBB0_463
	s_barrier

.LBB0_1346:
	s_ashr_i32 s17, s16, 31
	s_lshl_b64 s[24:25], s[16:17], 16
	s_add_i32 s17, s50, 0x80
	v_add_u32_e32 v202, s17, v1
	v_add_u32_e32 v203, s17, v190
	s_lshl_b32 s17, s16, 2
	s_add_i32 s17, s17, 0
	s_add_i32 s17, s17, 0x20000
	s_add_u32 s24, s18, s24
	s_addc_u32 s25, s19, s25
	v_mov_b32_e32 v175, v167
	v_mov_b32_e32 v173, v167
	s_add_u32 s56, s26, 0x100
	v_add_u32_e32 v200, s50, v1
	v_add_u32_e32 v201, s50, v190
	v_lshl_add_u64 v[178:179], s[10:11], 0, v[172:173]
	v_lshl_add_u64 v[180:181], s[10:11], 0, v[174:175]
	s_addc_u32 s57, s27, 0
	s_mov_b32 s58, -2
	s_mov_b64 s[26:27], 0
	s_xor_b64 s[28:29], s[22:23], -1
	v_mov_b32_e32 v169, v199
	v_mov_b32_e32 v171, v176
	v_mov_b32_e32 v173, v174
	v_mov_b32_e32 v175, v172
	s_add_u32 s30, s84, s26
	s_addc_u32 s31, s85, s27
	v_add_u32_e32 v2, s3, v193
	v_add_u32_e32 v14, s2, v193
	s_add_u32 s34, s30, 0x35400100
	ds_read_b128 v[18:21], v2
	ds_read_b128 v[22:25], v2 offset:1024
	ds_read_b128 v[26:29], v2 offset:2048
	ds_read_b128 v[30:33], v2 offset:3072
	ds_read_b128 v[2:5], v14
	ds_read_b128 v[6:9], v14 offset:1024
	ds_read_b128 v[10:13], v14 offset:2048
	ds_read_b128 v[14:17], v14 offset:3072
	s_addc_u32 s35, s31, 0
	s_add_u32 s59, s56, s26
	s_addc_u32 s60, s57, s27
	s_cmpk_eq_i32 s26, 0x700
	s_cselect_b64 vcc, -1, 0
	s_and_b64 s[30:31], vcc, exec
	v_cndmask_b32_e32 v166, v199, v169, vcc
	s_cselect_b32 s35, s5, s35
	s_cselect_b32 s34, s4, s34
	v_cndmask_b32_e32 v238, v176, v171, vcc
	v_cndmask_b32_e32 v229, v174, v173, vcc
	v_cndmask_b32_e32 v240, v172, v175, vcc
	s_cselect_b32 s31, s21, s60
	s_cselect_b32 s30, s20, s59
	v_lshl_add_u64 v[230:231], v[180:181], 0, s[26:27]
	s_add_i32 m0, s39, 0xc000
	ds_read_b128 v[182:185], v197
	ds_read_b128 v[186:189], v197 offset:1024
	ds_read_b128 v[204:207], v197 offset:2048
	ds_read_b128 v[208:211], v197 offset:3072
	ds_read_b128 v[212:215], v197 offset:4096
	ds_read_b128 v[216:219], v197 offset:5120
	ds_read_b128 v[220:223], v197 offset:6144
	ds_read_b128 v[224:227], v197 offset:7168
	global_load_lds_dwordx4 v[230:231], off
	v_lshl_add_u64 v[230:231], v[178:179], 0, s[26:27]
	s_add_i32 m0, s39, 0xe000
	s_nop 0
	global_load_lds_dwordx4 v[230:231], off
	s_waitcnt vmcnt(8)
	s_waitcnt lgkmcnt(0)
	s_barrier
	s_setprio 1
	s_waitcnt lgkmcnt(0)
	s_nop 1
	v_mfma_f32_16x16x128_f8f6f4 v[158:161], v[18:25], v[182:189], 0
	v_mfma_f32_16x16x128_f8f6f4 v[150:153], v[26:33], v[182:189], 0
	v_mfma_f32_16x16x128_f8f6f4 v[142:145], v[18:25], v[204:211], 0
	v_mfma_f32_16x16x128_f8f6f4 v[134:137], v[26:33], v[204:211], 0
	v_mfma_f32_16x16x128_f8f6f4 v[126:129], v[18:25], v[212:219], 0
	v_mfma_f32_16x16x128_f8f6f4 v[118:121], v[26:33], v[212:219], 0
	v_mfma_f32_16x16x128_f8f6f4 v[110:113], v[18:25], v[220:227], 0
	v_mfma_f32_16x16x128_f8f6f4 v[102:105], v[26:33], v[220:227], 0
	s_setprio 0
	s_setprio 1
	s_nop 1
	v_mfma_f32_16x16x128_f8f6f4 v[154:157], v[2:9], v[182:189], 0
	v_mfma_f32_16x16x128_f8f6f4 v[146:149], v[10:17], v[182:189], 0
	v_mfma_f32_16x16x128_f8f6f4 v[138:141], v[2:9], v[204:211], 0
	v_mfma_f32_16x16x128_f8f6f4 v[130:133], v[10:17], v[204:211], 0
	v_mfma_f32_16x16x128_f8f6f4 v[122:125], v[2:9], v[212:219], 0
	v_mfma_f32_16x16x128_f8f6f4 v[114:117], v[10:17], v[212:219], 0
	v_mfma_f32_16x16x128_f8f6f4 v[106:109], v[2:9], v[220:227], 0
	v_mfma_f32_16x16x128_f8f6f4 v[98:101], v[10:17], v[220:227], 0
	s_setprio 0
	s_barrier
	s_add_i32 s59, s3, s38
	v_lshl_add_u64 v[182:183], s[30:31], 0, v[164:165]
	s_mov_b32 m0, s59
	ds_read_b128 v[204:207], v197 offset:16384
	ds_read_b128 v[208:211], v197 offset:17408
	ds_read_b128 v[212:215], v197 offset:18432
	ds_read_b128 v[216:219], v197 offset:19456
	ds_read_b128 v[220:223], v197 offset:20480
	ds_read_b128 v[224:227], v197 offset:21504
	ds_read_b128 v[230:233], v197 offset:22528
	ds_read_b128 v[234:237], v197 offset:23552
	global_load_lds_dwordx4 v[182:183], off
	s_add_i32 m0, s59, 0x2000
	s_add_u32 s60, s30, 0x40000
	v_lshl_add_u64 v[184:185], s[30:31], 0, v[162:163]
	s_addc_u32 s61, s31, 0
	s_add_i32 s59, s2, s38
	global_load_lds_dwordx4 v[184:185], off
	v_lshl_add_u64 v[186:187], s[60:61], 0, v[164:165]
	s_mov_b32 m0, s59
	v_mov_b32_e32 v239, v167
	global_load_lds_dwordx4 v[186:187], off
	v_lshl_add_u64 v[186:187], s[60:61], 0, v[162:163]
	s_add_i32 m0, s59, 0x2000
	v_lshl_add_u64 v[188:189], s[34:35], 0, v[166:167]
	global_load_lds_dwordx4 v[186:187], off
	s_mov_b32 m0, s39
	v_lshl_add_u64 v[186:187], s[34:35], 0, v[238:239]
	global_load_lds_dwordx4 v166, s[34:35]
	s_mov_b32 m0, s40
	s_nop 0
	global_load_lds_dwordx4 v238, s[34:35]
	s_waitcnt vmcnt(8)
	s_waitcnt lgkmcnt(0)
	s_barrier
	s_setprio 1
	s_waitcnt lgkmcnt(0)
	s_nop 1
	v_mfma_f32_16x16x128_f8f6f4 v[94:97], v[18:25], v[204:211], 0
	v_mfma_f32_16x16x128_f8f6f4 v[86:89], v[26:33], v[204:211], 0
	v_mfma_f32_16x16x128_f8f6f4 v[78:81], v[18:25], v[212:219], 0
	v_mfma_f32_16x16x128_f8f6f4 v[66:69], v[26:33], v[212:219], 0
	v_mfma_f32_16x16x128_f8f6f4 v[54:57], v[18:25], v[220:227], 0
	v_mfma_f32_16x16x128_f8f6f4 v[46:49], v[26:33], v[220:227], 0
	v_mfma_f32_16x16x128_f8f6f4 v[38:41], v[18:25], v[230:237], 0
	v_mfma_f32_16x16x128_f8f6f4 v[34:37], v[26:33], v[230:237], 0
	s_setprio 0
	s_setprio 1
	s_nop 1
	v_mfma_f32_16x16x128_f8f6f4 v[90:93], v[2:9], v[204:211], 0
	v_mfma_f32_16x16x128_f8f6f4 v[82:85], v[10:17], v[204:211], 0
	v_mfma_f32_16x16x128_f8f6f4 v[74:77], v[2:9], v[212:219], 0
	v_mfma_f32_16x16x128_f8f6f4 v[58:61], v[10:17], v[212:219], 0
	v_mfma_f32_16x16x128_f8f6f4 v[70:73], v[2:9], v[220:227], 0
	v_mfma_f32_16x16x128_f8f6f4 v[62:65], v[10:17], v[220:227], 0
	v_mfma_f32_16x16x128_f8f6f4 v[50:53], v[2:9], v[230:237], 0
	v_mfma_f32_16x16x128_f8f6f4 v[42:45], v[10:17], v[230:237], 0
	s_setprio 0
	s_barrier
	v_add_u32_e32 v14, s86, v193
	v_add_u32_e32 v30, s87, v193
	ds_read_b128 v[2:5], v14
	ds_read_b128 v[6:9], v14 offset:1024
	ds_read_b128 v[10:13], v14 offset:2048
	ds_read_b128 v[14:17], v14 offset:3072
	ds_read_b128 v[18:21], v30
	ds_read_b128 v[22:25], v30 offset:1024
	ds_read_b128 v[26:29], v30 offset:2048
	ds_read_b128 v[30:33], v30 offset:3072
	s_mov_b32 m0, s41
	ds_read_b128 v[204:207], v197 offset:32768
	ds_read_b128 v[208:211], v197 offset:33792
	ds_read_b128 v[212:215], v197 offset:34816
	ds_read_b128 v[216:219], v197 offset:35840
	ds_read_b128 v[220:223], v197 offset:36864
	ds_read_b128 v[224:227], v197 offset:37888
	ds_read_b128 v[230:233], v197 offset:38912
	ds_read_b128 v[234:237], v197 offset:39936
	global_load_lds_dwordx4 v229, s[34:35]
	s_mov_b32 m0, s42
	s_nop 0
	global_load_lds_dwordx4 v240, s[34:35]
	s_waitcnt vmcnt(8)
	s_waitcnt lgkmcnt(0)
	s_barrier
	s_setprio 1
	s_waitcnt lgkmcnt(0)
	s_nop 1
	v_mfma_f32_16x16x128_f8f6f4 v[158:161], v[2:9], v[204:211], v[158:161]
	v_mfma_f32_16x16x128_f8f6f4 v[150:153], v[10:17], v[204:211], v[150:153]
	v_mfma_f32_16x16x128_f8f6f4 v[142:145], v[2:9], v[212:219], v[142:145]
	v_mfma_f32_16x16x128_f8f6f4 v[134:137], v[10:17], v[212:219], v[134:137]
	v_mfma_f32_16x16x128_f8f6f4 v[126:129], v[2:9], v[220:227], v[126:129]
	v_mfma_f32_16x16x128_f8f6f4 v[118:121], v[10:17], v[220:227], v[118:121]
	v_mfma_f32_16x16x128_f8f6f4 v[110:113], v[2:9], v[230:237], v[110:113]
	v_mfma_f32_16x16x128_f8f6f4 v[102:105], v[10:17], v[230:237], v[102:105]
	s_setprio 0
	s_setprio 1
	s_nop 1
	v_mfma_f32_16x16x128_f8f6f4 v[154:157], v[18:25], v[204:211], v[154:157]
	v_mfma_f32_16x16x128_f8f6f4 v[146:149], v[26:33], v[204:211], v[146:149]
	v_mfma_f32_16x16x128_f8f6f4 v[138:141], v[18:25], v[212:219], v[138:141]
	v_mfma_f32_16x16x128_f8f6f4 v[130:133], v[26:33], v[212:219], v[130:133]
	v_mfma_f32_16x16x128_f8f6f4 v[122:125], v[18:25], v[220:227], v[122:125]
	v_mfma_f32_16x16x128_f8f6f4 v[114:117], v[26:33], v[220:227], v[114:117]
	v_mfma_f32_16x16x128_f8f6f4 v[106:109], v[18:25], v[230:237], v[106:109]
	v_mfma_f32_16x16x128_f8f6f4 v[98:101], v[26:33], v[230:237], v[98:101]
	s_setprio 0
	s_barrier
	s_add_i32 s34, s86, s38
	v_lshl_add_u64 v[182:183], v[182:183], 0, s[8:9]
	s_mov_b32 m0, s34
	ds_read_b128 v[204:207], v197 offset:49152
	ds_read_b128 v[208:211], v197 offset:50176
	ds_read_b128 v[212:215], v197 offset:51200
	ds_read_b128 v[216:219], v197 offset:52224
	ds_read_b128 v[220:223], v197 offset:53248
	ds_read_b128 v[224:227], v197 offset:54272
	ds_read_b128 v[230:233], v197 offset:55296
	ds_read_b128 v[234:237], v197 offset:56320
	global_load_lds_dwordx4 v[182:183], off
	s_add_i32 m0, s34, 0x2000
	s_add_u32 s30, s30, 0x40080
	v_lshl_add_u64 v[182:183], v[184:185], 0, s[8:9]
	s_addc_u32 s31, s31, 0
	s_add_i32 s34, s87, s38
	global_load_lds_dwordx4 v[182:183], off
	v_lshl_add_u64 v[182:183], s[30:31], 0, v[164:165]
	s_mov_b32 m0, s34
	s_nop 0
	global_load_lds_dwordx4 v[182:183], off
	v_lshl_add_u64 v[182:183], s[30:31], 0, v[162:163]
	s_add_i32 m0, s34, 0x2000
	s_nop 0
	global_load_lds_dwordx4 v[182:183], off
	v_lshl_add_u64 v[182:183], v[188:189], 0, s[8:9]
	s_mov_b32 m0, s43
	s_nop 0
	global_load_lds_dwordx4 v[182:183], off
	v_lshl_add_u64 v[182:183], v[186:187], 0, s[8:9]
	s_mov_b32 m0, s44
	s_nop 0
	global_load_lds_dwordx4 v[182:183], off
	s_waitcnt vmcnt(8)
	s_waitcnt lgkmcnt(0)
	s_barrier
	s_setprio 1
	s_waitcnt lgkmcnt(0)
	s_nop 1
	v_mfma_f32_16x16x128_f8f6f4 v[94:97], v[2:9], v[204:211], v[94:97]
	v_mfma_f32_16x16x128_f8f6f4 v[86:89], v[10:17], v[204:211], v[86:89]
	v_mfma_f32_16x16x128_f8f6f4 v[78:81], v[2:9], v[212:219], v[78:81]
	v_mfma_f32_16x16x128_f8f6f4 v[66:69], v[10:17], v[212:219], v[66:69]
	v_mfma_f32_16x16x128_f8f6f4 v[54:57], v[2:9], v[220:227], v[54:57]
	v_mfma_f32_16x16x128_f8f6f4 v[46:49], v[10:17], v[220:227], v[46:49]
	v_mfma_f32_16x16x128_f8f6f4 v[38:41], v[2:9], v[230:237], v[38:41]
	v_mfma_f32_16x16x128_f8f6f4 v[34:37], v[10:17], v[230:237], v[34:37]
	s_setprio 0
	s_setprio 1
	s_nop 1
	v_mfma_f32_16x16x128_f8f6f4 v[90:93], v[18:25], v[204:211], v[90:93]
	v_mfma_f32_16x16x128_f8f6f4 v[82:85], v[26:33], v[204:211], v[82:85]
	v_mfma_f32_16x16x128_f8f6f4 v[74:77], v[18:25], v[212:219], v[74:77]
	v_mfma_f32_16x16x128_f8f6f4 v[58:61], v[26:33], v[212:219], v[58:61]
	v_mfma_f32_16x16x128_f8f6f4 v[70:73], v[18:25], v[220:227], v[70:73]
	v_mfma_f32_16x16x128_f8f6f4 v[62:65], v[26:33], v[220:227], v[62:65]
	v_mfma_f32_16x16x128_f8f6f4 v[50:53], v[18:25], v[230:237], v[50:53]
	v_mfma_f32_16x16x128_f8f6f4 v[42:45], v[26:33], v[230:237], v[42:45]
	s_setprio 0
	s_barrier
	s_add_i32 s58, s58, 2
	s_add_u32 s26, s26, 0x100
	s_addc_u32 s27, s27, 0
	s_cmp_gt_u32 s58, 13
	s_cbranch_scc1 .LBB0_1350
	s_branch .LBB0_1348

.LBB0_1418:
	s_add_u32 s26, s26, 0x80
	s_addc_u32 s27, s27, 0
	s_add_u32 s34, s30, 0x100
	s_addc_u32 s35, s31, 0
	s_mov_b32 s50, -2
	ds_read_b128 v[18:21], v192
	ds_read_b128 v[22:25], v192 offset:1024
	ds_read_b128 v[26:29], v192 offset:2048
	ds_read_b128 v[30:33], v192 offset:3072
	ds_read_b128 v[2:5], v193
	ds_read_b128 v[6:9], v193 offset:1024
	ds_read_b128 v[10:13], v193 offset:2048
	ds_read_b128 v[14:17], v193 offset:3072
	s_add_u32 s28, s26, 0x80
	s_addc_u32 s29, s27, 0
	s_cmp_eq_u32 s50, 12
	s_cselect_b32 s31, s19, s29
	s_cselect_b32 s30, s18, s28
	s_cselect_b32 s29, s21, s35
	s_cselect_b32 s28, s20, s34
	v_lshl_add_u64 v[220:221], s[26:27], 0, v[178:179]
	s_add_i32 m0, s38, 0xc000
	ds_read_b128 v[180:183], v194
	ds_read_b128 v[184:187], v194 offset:1024
	ds_read_b128 v[196:199], v194 offset:2048
	ds_read_b128 v[200:203], v194 offset:3072
	ds_read_b128 v[204:207], v194 offset:4096
	ds_read_b128 v[208:211], v194 offset:5120
	ds_read_b128 v[212:215], v194 offset:6144
	ds_read_b128 v[216:219], v194 offset:7168
	global_load_lds_dwordx4 v[220:221], off
	v_lshl_add_u64 v[220:221], s[26:27], 0, v[176:177]
	s_add_i32 m0, s38, 0xe000
	s_nop 0
	global_load_lds_dwordx4 v[220:221], off
	s_waitcnt vmcnt(8)
	s_waitcnt lgkmcnt(0)
	s_barrier
	s_setprio 1
	s_waitcnt lgkmcnt(0)
	s_nop 1
	v_mfma_f32_16x16x128_f8f6f4 v[158:161], v[18:25], v[180:187], 0
	v_mfma_f32_16x16x128_f8f6f4 v[154:157], v[26:33], v[180:187], 0
	v_mfma_f32_16x16x128_f8f6f4 v[142:145], v[18:25], v[196:203], 0
	v_mfma_f32_16x16x128_f8f6f4 v[138:141], v[26:33], v[196:203], 0
	v_mfma_f32_16x16x128_f8f6f4 v[126:129], v[18:25], v[204:211], 0
	v_mfma_f32_16x16x128_f8f6f4 v[122:125], v[26:33], v[204:211], 0
	v_mfma_f32_16x16x128_f8f6f4 v[110:113], v[18:25], v[212:219], 0
	v_mfma_f32_16x16x128_f8f6f4 v[106:109], v[26:33], v[212:219], 0
	s_setprio 0
	s_setprio 1
	s_nop 1
	v_mfma_f32_16x16x128_f8f6f4 v[150:153], v[2:9], v[180:187], 0
	v_mfma_f32_16x16x128_f8f6f4 v[146:149], v[10:17], v[180:187], 0
	v_mfma_f32_16x16x128_f8f6f4 v[134:137], v[2:9], v[196:203], 0
	v_mfma_f32_16x16x128_f8f6f4 v[130:133], v[10:17], v[196:203], 0
	v_mfma_f32_16x16x128_f8f6f4 v[118:121], v[2:9], v[204:211], 0
	v_mfma_f32_16x16x128_f8f6f4 v[114:117], v[10:17], v[204:211], 0
	v_mfma_f32_16x16x128_f8f6f4 v[94:97], v[2:9], v[212:219], 0
	v_mfma_f32_16x16x128_f8f6f4 v[90:93], v[10:17], v[212:219], 0
	s_setprio 0
	s_barrier
	s_add_i32 s51, s3, s37
	v_lshl_add_u64 v[180:181], s[28:29], 0, v[164:165]
	s_mov_b32 m0, s51
	ds_read_b128 v[196:199], v194 offset:16384
	ds_read_b128 v[200:203], v194 offset:17408
	ds_read_b128 v[204:207], v194 offset:18432
	ds_read_b128 v[208:211], v194 offset:19456
	ds_read_b128 v[212:215], v194 offset:20480
	ds_read_b128 v[216:219], v194 offset:21504
	ds_read_b128 v[220:223], v194 offset:22528
	ds_read_b128 v[224:227], v194 offset:23552
	global_load_lds_dwordx4 v[180:181], off
	s_add_i32 m0, s51, 0x2000
	s_add_u32 s52, s28, 0x40000
	v_lshl_add_u64 v[182:183], s[28:29], 0, v[162:163]
	s_addc_u32 s53, s29, 0
	s_add_i32 s51, s2, s37
	global_load_lds_dwordx4 v[182:183], off
	v_lshl_add_u64 v[184:185], s[52:53], 0, v[164:165]
	s_mov_b32 m0, s51
	v_lshl_add_u64 v[186:187], s[30:31], 0, v[168:169]
	global_load_lds_dwordx4 v[184:185], off
	v_lshl_add_u64 v[184:185], s[52:53], 0, v[162:163]
	s_add_i32 m0, s51, 0x2000
	s_nop 0
	global_load_lds_dwordx4 v[184:185], off
	v_lshl_add_u64 v[184:185], s[30:31], 0, v[166:167]
	s_mov_b32 m0, s38
	s_nop 0
	global_load_lds_dwordx4 v[184:185], off
	s_mov_b32 m0, s39
	s_nop 0
	global_load_lds_dwordx4 v[186:187], off
	s_waitcnt vmcnt(8)
	s_waitcnt lgkmcnt(0)
	s_barrier
	s_setprio 1
	s_waitcnt lgkmcnt(0)
	s_nop 1
	v_mfma_f32_16x16x128_f8f6f4 v[78:81], v[18:25], v[196:203], 0
	v_mfma_f32_16x16x128_f8f6f4 v[74:77], v[26:33], v[196:203], 0
	v_mfma_f32_16x16x128_f8f6f4 v[62:65], v[18:25], v[204:211], 0
	v_mfma_f32_16x16x128_f8f6f4 v[58:61], v[26:33], v[204:211], 0
	v_mfma_f32_16x16x128_f8f6f4 v[46:49], v[18:25], v[212:219], 0
	v_mfma_f32_16x16x128_f8f6f4 v[42:45], v[26:33], v[212:219], 0
	v_mfma_f32_16x16x128_f8f6f4 v[38:41], v[18:25], v[220:227], 0
	v_mfma_f32_16x16x128_f8f6f4 v[34:37], v[26:33], v[220:227], 0
	s_setprio 0
	s_setprio 1
	s_nop 1
	v_mfma_f32_16x16x128_f8f6f4 v[98:101], v[2:9], v[196:203], 0
	v_mfma_f32_16x16x128_f8f6f4 v[102:105], v[10:17], v[196:203], 0
	v_mfma_f32_16x16x128_f8f6f4 v[82:85], v[2:9], v[204:211], 0
	v_mfma_f32_16x16x128_f8f6f4 v[86:89], v[10:17], v[204:211], 0
	v_mfma_f32_16x16x128_f8f6f4 v[66:69], v[2:9], v[212:219], 0
	v_mfma_f32_16x16x128_f8f6f4 v[70:73], v[10:17], v[212:219], 0
	v_mfma_f32_16x16x128_f8f6f4 v[50:53], v[2:9], v[220:227], 0
	v_mfma_f32_16x16x128_f8f6f4 v[54:57], v[10:17], v[220:227], 0
	s_setprio 0
	s_barrier
	v_add_u32_e32 v14, s86, v188
	v_add_u32_e32 v30, s87, v188
	ds_read_b128 v[2:5], v14
	ds_read_b128 v[6:9], v14 offset:1024
	ds_read_b128 v[10:13], v14 offset:2048
	ds_read_b128 v[14:17], v14 offset:3072
	ds_read_b128 v[18:21], v30
	ds_read_b128 v[22:25], v30 offset:1024
	ds_read_b128 v[26:29], v30 offset:2048
	ds_read_b128 v[30:33], v30 offset:3072
	s_mov_b32 m0, s40
	v_lshl_add_u64 v[230:231], s[30:31], 0, v[170:171]
	ds_read_b128 v[196:199], v194 offset:32768
	ds_read_b128 v[200:203], v194 offset:33792
	ds_read_b128 v[204:207], v194 offset:34816
	ds_read_b128 v[208:211], v194 offset:35840
	ds_read_b128 v[212:215], v194 offset:36864
	ds_read_b128 v[216:219], v194 offset:37888
	ds_read_b128 v[220:223], v194 offset:38912
	ds_read_b128 v[224:227], v194 offset:39936
	global_load_lds_dwordx4 v[230:231], off
	v_lshl_add_u64 v[230:231], s[30:31], 0, v[172:173]
	s_mov_b32 m0, s41
	s_nop 0
	global_load_lds_dwordx4 v[230:231], off
	s_waitcnt vmcnt(8)
	s_waitcnt lgkmcnt(0)
	s_barrier
	s_setprio 1
	s_waitcnt lgkmcnt(0)
	s_nop 1
	v_mfma_f32_16x16x128_f8f6f4 v[158:161], v[2:9], v[196:203], v[158:161]
	v_mfma_f32_16x16x128_f8f6f4 v[154:157], v[10:17], v[196:203], v[154:157]
	v_mfma_f32_16x16x128_f8f6f4 v[142:145], v[2:9], v[204:211], v[142:145]
	v_mfma_f32_16x16x128_f8f6f4 v[138:141], v[10:17], v[204:211], v[138:141]
	v_mfma_f32_16x16x128_f8f6f4 v[126:129], v[2:9], v[212:219], v[126:129]
	v_mfma_f32_16x16x128_f8f6f4 v[122:125], v[10:17], v[212:219], v[122:125]
	v_mfma_f32_16x16x128_f8f6f4 v[110:113], v[2:9], v[220:227], v[110:113]
	v_mfma_f32_16x16x128_f8f6f4 v[106:109], v[10:17], v[220:227], v[106:109]
	s_setprio 0
	s_setprio 1
	s_nop 1
	v_mfma_f32_16x16x128_f8f6f4 v[150:153], v[18:25], v[196:203], v[150:153]
	v_mfma_f32_16x16x128_f8f6f4 v[146:149], v[26:33], v[196:203], v[146:149]
	v_mfma_f32_16x16x128_f8f6f4 v[134:137], v[18:25], v[204:211], v[134:137]
	v_mfma_f32_16x16x128_f8f6f4 v[130:133], v[26:33], v[204:211], v[130:133]
	v_mfma_f32_16x16x128_f8f6f4 v[118:121], v[18:25], v[212:219], v[118:121]
	v_mfma_f32_16x16x128_f8f6f4 v[114:117], v[26:33], v[212:219], v[114:117]
	v_mfma_f32_16x16x128_f8f6f4 v[94:97], v[18:25], v[220:227], v[94:97]
	v_mfma_f32_16x16x128_f8f6f4 v[90:93], v[26:33], v[220:227], v[90:93]
	s_setprio 0
	s_barrier
	s_add_i32 s30, s86, s37
	v_lshl_add_u64 v[180:181], v[180:181], 0, s[8:9]
	s_mov_b32 m0, s30
	ds_read_b128 v[196:199], v194 offset:49152
	ds_read_b128 v[200:203], v194 offset:50176
	ds_read_b128 v[204:207], v194 offset:51200
	ds_read_b128 v[208:211], v194 offset:52224
	ds_read_b128 v[212:215], v194 offset:53248
	ds_read_b128 v[216:219], v194 offset:54272
	ds_read_b128 v[220:223], v194 offset:55296
	ds_read_b128 v[224:227], v194 offset:56320
	global_load_lds_dwordx4 v[180:181], off
	s_add_i32 m0, s30, 0x2000
	s_add_u32 s28, s28, 0x40080
	v_lshl_add_u64 v[180:181], v[182:183], 0, s[8:9]
	s_addc_u32 s29, s29, 0
	s_add_i32 s30, s87, s37
	global_load_lds_dwordx4 v[180:181], off
	v_lshl_add_u64 v[180:181], s[28:29], 0, v[164:165]
	s_mov_b32 m0, s30
	s_nop 0
	global_load_lds_dwordx4 v[180:181], off
	v_lshl_add_u64 v[180:181], s[28:29], 0, v[162:163]
	s_add_i32 m0, s30, 0x2000
	s_nop 0
	global_load_lds_dwordx4 v[180:181], off
	v_lshl_add_u64 v[180:181], v[184:185], 0, s[8:9]
	s_mov_b32 m0, s43
	s_nop 0
	global_load_lds_dwordx4 v[180:181], off
	v_lshl_add_u64 v[180:181], v[186:187], 0, s[8:9]
	s_mov_b32 m0, s44
	s_nop 0
	global_load_lds_dwordx4 v[180:181], off
	s_waitcnt vmcnt(8)
	s_waitcnt lgkmcnt(0)
	s_barrier
	s_setprio 1
	s_waitcnt lgkmcnt(0)
	s_nop 1
	v_mfma_f32_16x16x128_f8f6f4 v[78:81], v[2:9], v[196:203], v[78:81]
	v_mfma_f32_16x16x128_f8f6f4 v[74:77], v[10:17], v[196:203], v[74:77]
	v_mfma_f32_16x16x128_f8f6f4 v[62:65], v[2:9], v[204:211], v[62:65]
	v_mfma_f32_16x16x128_f8f6f4 v[58:61], v[10:17], v[204:211], v[58:61]
	v_mfma_f32_16x16x128_f8f6f4 v[46:49], v[2:9], v[212:219], v[46:49]
	v_mfma_f32_16x16x128_f8f6f4 v[42:45], v[10:17], v[212:219], v[42:45]
	v_mfma_f32_16x16x128_f8f6f4 v[38:41], v[2:9], v[220:227], v[38:41]
	v_mfma_f32_16x16x128_f8f6f4 v[34:37], v[10:17], v[220:227], v[34:37]
	s_setprio 0
	s_setprio 1
	s_nop 1
	v_mfma_f32_16x16x128_f8f6f4 v[98:101], v[18:25], v[196:203], v[98:101]
	v_mfma_f32_16x16x128_f8f6f4 v[102:105], v[26:33], v[196:203], v[102:105]
	v_mfma_f32_16x16x128_f8f6f4 v[82:85], v[18:25], v[204:211], v[82:85]
	v_mfma_f32_16x16x128_f8f6f4 v[86:89], v[26:33], v[204:211], v[86:89]
	v_mfma_f32_16x16x128_f8f6f4 v[66:69], v[18:25], v[212:219], v[66:69]
	v_mfma_f32_16x16x128_f8f6f4 v[70:73], v[26:33], v[212:219], v[70:73]
	v_mfma_f32_16x16x128_f8f6f4 v[50:53], v[18:25], v[220:227], v[50:53]
	v_mfma_f32_16x16x128_f8f6f4 v[54:57], v[26:33], v[220:227], v[54:57]
	s_setprio 0
	s_barrier
	s_add_i32 s50, s50, 2
	s_add_u32 s26, s26, 0x100
	s_addc_u32 s27, s27, 0
	s_add_u32 s34, s34, 0x100
	s_addc_u32 s35, s35, 0
	s_cmp_gt_u32 s50, 13
	s_cbranch_scc0 .LBB0_1419
	s_branch .Lmy_pexit_p9
.LBB0_1419:
	ds_read_b128 v[18:21], v192
	ds_read_b128 v[22:25], v192 offset:1024
	ds_read_b128 v[26:29], v192 offset:2048
	ds_read_b128 v[30:33], v192 offset:3072
	ds_read_b128 v[2:5], v193
	ds_read_b128 v[6:9], v193 offset:1024
	ds_read_b128 v[10:13], v193 offset:2048
	ds_read_b128 v[14:17], v193 offset:3072
	s_add_u32 s28, s26, 0x80
	s_addc_u32 s29, s27, 0
	s_cmp_eq_u32 s50, 12
	s_cselect_b32 s31, s19, s29
	s_cselect_b32 s30, s18, s28
	s_cselect_b32 s29, s21, s35
	s_cselect_b32 s28, s20, s34
	v_lshl_add_u64 v[220:221], s[26:27], 0, v[178:179]
	s_add_i32 m0, s38, 0xc000
	ds_read_b128 v[180:183], v194
	ds_read_b128 v[184:187], v194 offset:1024
	ds_read_b128 v[196:199], v194 offset:2048
	ds_read_b128 v[200:203], v194 offset:3072
	ds_read_b128 v[204:207], v194 offset:4096
	ds_read_b128 v[208:211], v194 offset:5120
	ds_read_b128 v[212:215], v194 offset:6144
	ds_read_b128 v[216:219], v194 offset:7168
	global_load_lds_dwordx4 v[220:221], off
	v_lshl_add_u64 v[220:221], s[26:27], 0, v[176:177]
	s_add_i32 m0, s38, 0xe000
	s_nop 0
	global_load_lds_dwordx4 v[220:221], off
	s_waitcnt vmcnt(8)
	s_waitcnt lgkmcnt(0)
	s_barrier
	s_setprio 1
	s_waitcnt lgkmcnt(0)
	s_nop 1
	v_mfma_f32_16x16x128_f8f6f4 v[158:161], v[18:25], v[180:187], v[158:161]
	v_mfma_f32_16x16x128_f8f6f4 v[154:157], v[26:33], v[180:187], v[154:157]
	v_mfma_f32_16x16x128_f8f6f4 v[142:145], v[18:25], v[196:203], v[142:145]
	v_mfma_f32_16x16x128_f8f6f4 v[138:141], v[26:33], v[196:203], v[138:141]
	v_mfma_f32_16x16x128_f8f6f4 v[126:129], v[18:25], v[204:211], v[126:129]
	v_mfma_f32_16x16x128_f8f6f4 v[122:125], v[26:33], v[204:211], v[122:125]
	v_mfma_f32_16x16x128_f8f6f4 v[110:113], v[18:25], v[212:219], v[110:113]
	v_mfma_f32_16x16x128_f8f6f4 v[106:109], v[26:33], v[212:219], v[106:109]
	s_setprio 0
	s_setprio 1
	s_nop 1
	v_mfma_f32_16x16x128_f8f6f4 v[150:153], v[2:9], v[180:187], v[150:153]
	v_mfma_f32_16x16x128_f8f6f4 v[146:149], v[10:17], v[180:187], v[146:149]
	v_mfma_f32_16x16x128_f8f6f4 v[134:137], v[2:9], v[196:203], v[134:137]
	v_mfma_f32_16x16x128_f8f6f4 v[130:133], v[10:17], v[196:203], v[130:133]
	v_mfma_f32_16x16x128_f8f6f4 v[118:121], v[2:9], v[204:211], v[118:121]
	v_mfma_f32_16x16x128_f8f6f4 v[114:117], v[10:17], v[204:211], v[114:117]
	v_mfma_f32_16x16x128_f8f6f4 v[94:97], v[2:9], v[212:219], v[94:97]
	v_mfma_f32_16x16x128_f8f6f4 v[90:93], v[10:17], v[212:219], v[90:93]
	s_setprio 0
	s_barrier
	s_add_i32 s51, s3, s37
	v_lshl_add_u64 v[180:181], s[28:29], 0, v[164:165]
	s_mov_b32 m0, s51
	ds_read_b128 v[196:199], v194 offset:16384
	ds_read_b128 v[200:203], v194 offset:17408
	ds_read_b128 v[204:207], v194 offset:18432
	ds_read_b128 v[208:211], v194 offset:19456
	ds_read_b128 v[212:215], v194 offset:20480
	ds_read_b128 v[216:219], v194 offset:21504
	ds_read_b128 v[220:223], v194 offset:22528
	ds_read_b128 v[224:227], v194 offset:23552
	global_load_lds_dwordx4 v[180:181], off
	s_add_i32 m0, s51, 0x2000
	s_add_u32 s52, s28, 0x40000
	v_lshl_add_u64 v[182:183], s[28:29], 0, v[162:163]
	s_addc_u32 s53, s29, 0
	s_add_i32 s51, s2, s37
	global_load_lds_dwordx4 v[182:183], off
	v_lshl_add_u64 v[184:185], s[52:53], 0, v[164:165]
	s_mov_b32 m0, s51
	v_lshl_add_u64 v[186:187], s[30:31], 0, v[168:169]
	global_load_lds_dwordx4 v[184:185], off
	v_lshl_add_u64 v[184:185], s[52:53], 0, v[162:163]
	s_add_i32 m0, s51, 0x2000
	s_nop 0
	global_load_lds_dwordx4 v[184:185], off
	v_lshl_add_u64 v[184:185], s[30:31], 0, v[166:167]
	s_mov_b32 m0, s38
	s_nop 0
	global_load_lds_dwordx4 v[184:185], off
	s_mov_b32 m0, s39
	s_nop 0
	global_load_lds_dwordx4 v[186:187], off
	s_waitcnt vmcnt(8)
	s_waitcnt lgkmcnt(0)
	s_barrier
	s_setprio 1
	s_waitcnt lgkmcnt(0)
	s_nop 1
	v_mfma_f32_16x16x128_f8f6f4 v[78:81], v[18:25], v[196:203], v[78:81]
	v_mfma_f32_16x16x128_f8f6f4 v[74:77], v[26:33], v[196:203], v[74:77]
	v_mfma_f32_16x16x128_f8f6f4 v[62:65], v[18:25], v[204:211], v[62:65]
	v_mfma_f32_16x16x128_f8f6f4 v[58:61], v[26:33], v[204:211], v[58:61]
	v_mfma_f32_16x16x128_f8f6f4 v[46:49], v[18:25], v[212:219], v[46:49]
	v_mfma_f32_16x16x128_f8f6f4 v[42:45], v[26:33], v[212:219], v[42:45]
	v_mfma_f32_16x16x128_f8f6f4 v[38:41], v[18:25], v[220:227], v[38:41]
	v_mfma_f32_16x16x128_f8f6f4 v[34:37], v[26:33], v[220:227], v[34:37]
	s_setprio 0
	s_setprio 1
	s_nop 1
	v_mfma_f32_16x16x128_f8f6f4 v[98:101], v[2:9], v[196:203], v[98:101]
	v_mfma_f32_16x16x128_f8f6f4 v[102:105], v[10:17], v[196:203], v[102:105]
	v_mfma_f32_16x16x128_f8f6f4 v[82:85], v[2:9], v[204:211], v[82:85]
	v_mfma_f32_16x16x128_f8f6f4 v[86:89], v[10:17], v[204:211], v[86:89]
	v_mfma_f32_16x16x128_f8f6f4 v[66:69], v[2:9], v[212:219], v[66:69]
	v_mfma_f32_16x16x128_f8f6f4 v[70:73], v[10:17], v[212:219], v[70:73]
	v_mfma_f32_16x16x128_f8f6f4 v[50:53], v[2:9], v[220:227], v[50:53]
	v_mfma_f32_16x16x128_f8f6f4 v[54:57], v[10:17], v[220:227], v[54:57]
	s_setprio 0
	s_barrier
	v_add_u32_e32 v14, s86, v188
	v_add_u32_e32 v30, s87, v188
	ds_read_b128 v[2:5], v14
	ds_read_b128 v[6:9], v14 offset:1024
	ds_read_b128 v[10:13], v14 offset:2048
	ds_read_b128 v[14:17], v14 offset:3072
	ds_read_b128 v[18:21], v30
	ds_read_b128 v[22:25], v30 offset:1024
	ds_read_b128 v[26:29], v30 offset:2048
	ds_read_b128 v[30:33], v30 offset:3072
	s_mov_b32 m0, s40
	v_lshl_add_u64 v[230:231], s[30:31], 0, v[170:171]
	ds_read_b128 v[196:199], v194 offset:32768
	ds_read_b128 v[200:203], v194 offset:33792
	ds_read_b128 v[204:207], v194 offset:34816
	ds_read_b128 v[208:211], v194 offset:35840
	ds_read_b128 v[212:215], v194 offset:36864
	ds_read_b128 v[216:219], v194 offset:37888
	ds_read_b128 v[220:223], v194 offset:38912
	ds_read_b128 v[224:227], v194 offset:39936
	global_load_lds_dwordx4 v[230:231], off
	v_lshl_add_u64 v[230:231], s[30:31], 0, v[172:173]
	s_mov_b32 m0, s41
	s_nop 0
	global_load_lds_dwordx4 v[230:231], off
	s_waitcnt vmcnt(8)
	s_waitcnt lgkmcnt(0)
	s_barrier
	s_setprio 1
	s_waitcnt lgkmcnt(0)
	s_nop 1
	v_mfma_f32_16x16x128_f8f6f4 v[158:161], v[2:9], v[196:203], v[158:161]
	v_mfma_f32_16x16x128_f8f6f4 v[154:157], v[10:17], v[196:203], v[154:157]
	v_mfma_f32_16x16x128_f8f6f4 v[142:145], v[2:9], v[204:211], v[142:145]
	v_mfma_f32_16x16x128_f8f6f4 v[138:141], v[10:17], v[204:211], v[138:141]
	v_mfma_f32_16x16x128_f8f6f4 v[126:129], v[2:9], v[212:219], v[126:129]
	v_mfma_f32_16x16x128_f8f6f4 v[122:125], v[10:17], v[212:219], v[122:125]
	v_mfma_f32_16x16x128_f8f6f4 v[110:113], v[2:9], v[220:227], v[110:113]
	v_mfma_f32_16x16x128_f8f6f4 v[106:109], v[10:17], v[220:227], v[106:109]
	s_setprio 0
	s_setprio 1
	s_nop 1
	v_mfma_f32_16x16x128_f8f6f4 v[150:153], v[18:25], v[196:203], v[150:153]
	v_mfma_f32_16x16x128_f8f6f4 v[146:149], v[26:33], v[196:203], v[146:149]
	v_mfma_f32_16x16x128_f8f6f4 v[134:137], v[18:25], v[204:211], v[134:137]
	v_mfma_f32_16x16x128_f8f6f4 v[130:133], v[26:33], v[204:211], v[130:133]
	v_mfma_f32_16x16x128_f8f6f4 v[118:121], v[18:25], v[212:219], v[118:121]
	v_mfma_f32_16x16x128_f8f6f4 v[114:117], v[26:33], v[212:219], v[114:117]
	v_mfma_f32_16x16x128_f8f6f4 v[94:97], v[18:25], v[220:227], v[94:97]
	v_mfma_f32_16x16x128_f8f6f4 v[90:93], v[26:33], v[220:227], v[90:93]
	s_setprio 0
	s_barrier
	s_add_i32 s30, s86, s37
	v_lshl_add_u64 v[180:181], v[180:181], 0, s[8:9]
	s_mov_b32 m0, s30
	ds_read_b128 v[196:199], v194 offset:49152
	ds_read_b128 v[200:203], v194 offset:50176
	ds_read_b128 v[204:207], v194 offset:51200
	ds_read_b128 v[208:211], v194 offset:52224
	ds_read_b128 v[212:215], v194 offset:53248
	ds_read_b128 v[216:219], v194 offset:54272
	ds_read_b128 v[220:223], v194 offset:55296
	ds_read_b128 v[224:227], v194 offset:56320
	global_load_lds_dwordx4 v[180:181], off
	s_add_i32 m0, s30, 0x2000
	s_add_u32 s28, s28, 0x40080
	v_lshl_add_u64 v[180:181], v[182:183], 0, s[8:9]
	s_addc_u32 s29, s29, 0
	s_add_i32 s30, s87, s37
	global_load_lds_dwordx4 v[180:181], off
	v_lshl_add_u64 v[180:181], s[28:29], 0, v[164:165]
	s_mov_b32 m0, s30
	s_nop 0
	global_load_lds_dwordx4 v[180:181], off
	v_lshl_add_u64 v[180:181], s[28:29], 0, v[162:163]
	s_add_i32 m0, s30, 0x2000
	s_nop 0
	global_load_lds_dwordx4 v[180:181], off
	v_lshl_add_u64 v[180:181], v[184:185], 0, s[8:9]
	s_mov_b32 m0, s43
	s_nop 0
	global_load_lds_dwordx4 v[180:181], off
	v_lshl_add_u64 v[180:181], v[186:187], 0, s[8:9]
	s_mov_b32 m0, s44
	s_nop 0
	global_load_lds_dwordx4 v[180:181], off
	s_waitcnt vmcnt(8)
	s_waitcnt lgkmcnt(0)
	s_barrier
	s_setprio 1
	s_waitcnt lgkmcnt(0)
	s_nop 1
	v_mfma_f32_16x16x128_f8f6f4 v[78:81], v[2:9], v[196:203], v[78:81]
	v_mfma_f32_16x16x128_f8f6f4 v[74:77], v[10:17], v[196:203], v[74:77]
	v_mfma_f32_16x16x128_f8f6f4 v[62:65], v[2:9], v[204:211], v[62:65]
	v_mfma_f32_16x16x128_f8f6f4 v[58:61], v[10:17], v[204:211], v[58:61]
	v_mfma_f32_16x16x128_f8f6f4 v[46:49], v[2:9], v[212:219], v[46:49]
	v_mfma_f32_16x16x128_f8f6f4 v[42:45], v[10:17], v[212:219], v[42:45]
	v_mfma_f32_16x16x128_f8f6f4 v[38:41], v[2:9], v[220:227], v[38:41]
	v_mfma_f32_16x16x128_f8f6f4 v[34:37], v[10:17], v[220:227], v[34:37]
	s_setprio 0
	s_setprio 1
	s_nop 1
	v_mfma_f32_16x16x128_f8f6f4 v[98:101], v[18:25], v[196:203], v[98:101]
	v_mfma_f32_16x16x128_f8f6f4 v[102:105], v[26:33], v[196:203], v[102:105]
	v_mfma_f32_16x16x128_f8f6f4 v[82:85], v[18:25], v[204:211], v[82:85]
	v_mfma_f32_16x16x128_f8f6f4 v[86:89], v[26:33], v[204:211], v[86:89]
	v_mfma_f32_16x16x128_f8f6f4 v[66:69], v[18:25], v[212:219], v[66:69]
	v_mfma_f32_16x16x128_f8f6f4 v[70:73], v[26:33], v[212:219], v[70:73]
	v_mfma_f32_16x16x128_f8f6f4 v[50:53], v[18:25], v[220:227], v[50:53]
	v_mfma_f32_16x16x128_f8f6f4 v[54:57], v[26:33], v[220:227], v[54:57]
	s_setprio 0
	s_barrier
	s_add_i32 s50, s50, 2
	s_add_u32 s26, s26, 0x100
	s_addc_u32 s27, s27, 0
	s_add_u32 s34, s34, 0x100
	s_addc_u32 s35, s35, 0
	s_cmp_gt_u32 s50, 13
	s_cbranch_scc0 .LBB0_1419
.Lmy_pexit_p9:
	s_and_b64 vcc, exec, s[14:15]
	s_cbranch_vccz .LBB0_1422
	s_barrier
.LBB0_1422:
	v_lshl_add_u32 v6, s25, 10, v189
	v_mov_b32_e32 v18, 0x3c800000
	s_nop 15
	s_nop 15
	ds_read_b128 v[10:13], v6
	ds_read_b128 v[14:17], v6 offset:16
	ds_read_b128 v[2:5], v6 offset:512
	ds_read_b128 v[6:9], v6 offset:528
	v_mov_b32_e32 v22, 0
	s_waitcnt lgkmcnt(0)
	v_pk_fma_f32 v[24:25], v[158:159], v[18:19], v[10:11] op_sel_hi:[1,0,1]
	v_pk_fma_f32 v[28:29], v[154:155], v[18:19], v[14:15] op_sel_hi:[1,0,1]
	v_mov_b32_e32 v23, 0
	v_cvt_pk_fp8_f32 v22, v24, v25
	v_cvt_pk_fp8_f32 v23, v28, v29
	v_pk_fma_f32 v[24:25], v[160:161], v[18:19], v[12:13] op_sel_hi:[1,0,1]
	v_pk_fma_f32 v[28:29], v[156:157], v[18:19], v[16:17] op_sel_hi:[1,0,1]
	v_cvt_pk_fp8_f32 v22, v24, v25 op_sel:[0,0,1]
	v_cvt_pk_fp8_f32 v23, v28, v29 op_sel:[0,0,1]
	v_pk_fma_f32 v[28:29], v[150:151], v[18:19], v[2:3] op_sel_hi:[1,0,1]
	v_pk_fma_f32 v[30:31], v[146:147], v[18:19], v[6:7] op_sel_hi:[1,0,1]
	v_mov_b32_e32 v24, 0
	v_mov_b32_e32 v25, 0
	v_cvt_pk_fp8_f32 v24, v28, v29
	v_cvt_pk_fp8_f32 v25, v30, v31
	v_lshl_add_u32 v26, s24, 8, v1
	v_ashrrev_i32_e32 v27, 31, v26
	v_lshlrev_b64 v[20:21], 11, v[26:27]
	s_lshl_b32 s24, s49, 8
	v_pk_fma_f32 v[28:29], v[152:153], v[18:19], v[4:5] op_sel_hi:[1,0,1]
	v_pk_fma_f32 v[30:31], v[148:149], v[18:19], v[8:9] op_sel_hi:[1,0,1]
	v_lshl_add_u64 v[20:21], s[4:5], 0, v[20:21]
	s_ashr_i32 s25, s24, 31
	v_cvt_pk_fp8_f32 v24, v28, v29 op_sel:[0,0,1]
	v_cvt_pk_fp8_f32 v25, v30, v31 op_sel:[0,0,1]
	v_lshl_add_u64 v[20:21], v[20:21], 0, s[24:25]
	v_lshl_add_u64 v[20:21], v[20:21], 0, s[10:11]
	v_lshl_add_u64 v[20:21], v[20:21], 0, v[174:175]
	global_store_dwordx4 v[20:21], v[22:25], off
	v_pk_fma_f32 v[30:31], v[138:139], v[18:19], v[14:15] op_sel_hi:[1,0,1]
	v_pk_fma_f32 v[32:33], v[130:131], v[18:19], v[6:7] op_sel_hi:[1,0,1]
	v_or_b32_e32 v22, 16, v26
	v_ashrrev_i32_e32 v23, 31, v22
	v_lshlrev_b64 v[22:23], 11, v[22:23]
	v_lshl_add_u64 v[28:29], s[4:5], 0, v[22:23]
	v_pk_fma_f32 v[24:25], v[142:143], v[18:19], v[10:11] op_sel_hi:[1,0,1]
	v_mov_b32_e32 v22, 0
	v_mov_b32_e32 v23, 0
	v_cvt_pk_fp8_f32 v22, v24, v25
	v_cvt_pk_fp8_f32 v23, v30, v31
	v_pk_fma_f32 v[24:25], v[144:145], v[18:19], v[12:13] op_sel_hi:[1,0,1]
	v_pk_fma_f32 v[30:31], v[140:141], v[18:19], v[16:17] op_sel_hi:[1,0,1]
	v_cvt_pk_fp8_f32 v22, v24, v25 op_sel:[0,0,1]
	v_cvt_pk_fp8_f32 v23, v30, v31 op_sel:[0,0,1]
	v_pk_fma_f32 v[30:31], v[134:135], v[18:19], v[2:3] op_sel_hi:[1,0,1]
	v_mov_b32_e32 v24, 0
	v_mov_b32_e32 v25, 0
	v_cvt_pk_fp8_f32 v24, v30, v31
	v_cvt_pk_fp8_f32 v25, v32, v33
	v_pk_fma_f32 v[30:31], v[136:137], v[18:19], v[4:5] op_sel_hi:[1,0,1]
	v_pk_fma_f32 v[32:33], v[132:133], v[18:19], v[8:9] op_sel_hi:[1,0,1]
	v_cvt_pk_fp8_f32 v24, v30, v31 op_sel:[0,0,1]
	v_cvt_pk_fp8_f32 v25, v32, v33 op_sel:[0,0,1]
	v_lshl_add_u64 v[28:29], v[28:29], 0, s[24:25]
	v_lshl_add_u64 v[28:29], v[28:29], 0, s[10:11]
	v_lshl_add_u64 v[28:29], v[28:29], 0, v[174:175]
	global_store_dwordx4 v[28:29], v[22:25], off
	v_pk_fma_f32 v[30:31], v[122:123], v[18:19], v[14:15] op_sel_hi:[1,0,1]
	v_pk_fma_f32 v[32:33], v[114:115], v[18:19], v[6:7] op_sel_hi:[1,0,1]
	v_or_b32_e32 v22, 32, v26
	v_ashrrev_i32_e32 v23, 31, v22
	v_lshlrev_b64 v[22:23], 11, v[22:23]
	v_lshl_add_u64 v[28:29], s[4:5], 0, v[22:23]
	v_pk_fma_f32 v[24:25], v[126:127], v[18:19], v[10:11] op_sel_hi:[1,0,1]
	v_mov_b32_e32 v22, 0
	v_mov_b32_e32 v23, 0
	v_cvt_pk_fp8_f32 v22, v24, v25
	v_cvt_pk_fp8_f32 v23, v30, v31
	v_pk_fma_f32 v[24:25], v[128:129], v[18:19], v[12:13] op_sel_hi:[1,0,1]
	v_pk_fma_f32 v[30:31], v[124:125], v[18:19], v[16:17] op_sel_hi:[1,0,1]
	v_cvt_pk_fp8_f32 v22, v24, v25 op_sel:[0,0,1]
	v_cvt_pk_fp8_f32 v23, v30, v31 op_sel:[0,0,1]
	v_pk_fma_f32 v[30:31], v[118:119], v[18:19], v[2:3] op_sel_hi:[1,0,1]
	v_mov_b32_e32 v24, 0
	v_mov_b32_e32 v25, 0
	v_cvt_pk_fp8_f32 v24, v30, v31
	v_cvt_pk_fp8_f32 v25, v32, v33
	v_pk_fma_f32 v[30:31], v[120:121], v[18:19], v[4:5] op_sel_hi:[1,0,1]
	v_pk_fma_f32 v[32:33], v[116:117], v[18:19], v[8:9] op_sel_hi:[1,0,1]
	v_cvt_pk_fp8_f32 v24, v30, v31 op_sel:[0,0,1]
	v_cvt_pk_fp8_f32 v25, v32, v33 op_sel:[0,0,1]
	v_lshl_add_u64 v[28:29], v[28:29], 0, s[24:25]
	v_lshl_add_u64 v[28:29], v[28:29], 0, s[10:11]
	v_lshl_add_u64 v[28:29], v[28:29], 0, v[174:175]
	global_store_dwordx4 v[28:29], v[22:25], off
	v_pk_fma_f32 v[28:29], v[106:107], v[18:19], v[14:15] op_sel_hi:[1,0,1]
	v_pk_fma_f32 v[30:31], v[90:91], v[18:19], v[6:7] op_sel_hi:[1,0,1]
	v_or_b32_e32 v22, 48, v26
	v_ashrrev_i32_e32 v23, 31, v22
	v_lshlrev_b64 v[22:23], 11, v[22:23]
	v_lshl_add_u64 v[26:27], s[4:5], 0, v[22:23]
	v_pk_fma_f32 v[24:25], v[110:111], v[18:19], v[10:11] op_sel_hi:[1,0,1]
	v_mov_b32_e32 v22, 0
	v_mov_b32_e32 v23, 0
	v_cvt_pk_fp8_f32 v22, v24, v25
	v_cvt_pk_fp8_f32 v23, v28, v29
	v_pk_fma_f32 v[24:25], v[112:113], v[18:19], v[12:13] op_sel_hi:[1,0,1]
	v_pk_fma_f32 v[28:29], v[108:109], v[18:19], v[16:17] op_sel_hi:[1,0,1]
	v_cvt_pk_fp8_f32 v22, v24, v25 op_sel:[0,0,1]
	v_cvt_pk_fp8_f32 v23, v28, v29 op_sel:[0,0,1]
	v_pk_fma_f32 v[28:29], v[94:95], v[18:19], v[2:3] op_sel_hi:[1,0,1]
	v_mov_b32_e32 v24, 0
	v_mov_b32_e32 v25, 0
	v_cvt_pk_fp8_f32 v24, v28, v29
	v_cvt_pk_fp8_f32 v25, v30, v31
	v_pk_fma_f32 v[28:29], v[96:97], v[18:19], v[4:5] op_sel_hi:[1,0,1]
	v_pk_fma_f32 v[30:31], v[92:93], v[18:19], v[8:9] op_sel_hi:[1,0,1]
	v_cvt_pk_fp8_f32 v24, v28, v29 op_sel:[0,0,1]
	v_cvt_pk_fp8_f32 v25, v30, v31 op_sel:[0,0,1]
	v_lshl_add_u64 v[26:27], v[26:27], 0, s[24:25]
	v_lshl_add_u64 v[26:27], v[26:27], 0, s[10:11]
	v_lshl_add_u64 v[26:27], v[26:27], 0, v[174:175]
	global_store_dwordx4 v[26:27], v[22:25], off
	v_pk_fma_f32 v[26:27], v[74:75], v[18:19], v[14:15] op_sel_hi:[1,0,1]
	v_pk_fma_f32 v[28:29], v[102:103], v[18:19], v[6:7] op_sel_hi:[1,0,1]
	v_pk_fma_f32 v[24:25], v[78:79], v[18:19], v[10:11] op_sel_hi:[1,0,1]
	v_mov_b32_e32 v22, 0
	v_mov_b32_e32 v23, 0
	v_cvt_pk_fp8_f32 v22, v24, v25
	v_cvt_pk_fp8_f32 v23, v26, v27
	v_pk_fma_f32 v[24:25], v[80:81], v[18:19], v[12:13] op_sel_hi:[1,0,1]
	v_pk_fma_f32 v[26:27], v[76:77], v[18:19], v[16:17] op_sel_hi:[1,0,1]
	v_cvt_pk_fp8_f32 v22, v24, v25 op_sel:[0,0,1]
	v_cvt_pk_fp8_f32 v23, v26, v27 op_sel:[0,0,1]
	v_pk_fma_f32 v[26:27], v[98:99], v[18:19], v[2:3] op_sel_hi:[1,0,1]
	v_mov_b32_e32 v24, 0
	v_mov_b32_e32 v25, 0
	v_cvt_pk_fp8_f32 v24, v26, v27
	v_cvt_pk_fp8_f32 v25, v28, v29
	v_pk_fma_f32 v[26:27], v[100:101], v[18:19], v[4:5] op_sel_hi:[1,0,1]
	v_pk_fma_f32 v[28:29], v[104:105], v[18:19], v[8:9] op_sel_hi:[1,0,1]
	v_cvt_pk_fp8_f32 v24, v26, v27 op_sel:[0,0,1]
	v_cvt_pk_fp8_f32 v25, v28, v29 op_sel:[0,0,1]
	v_add_co_u32_e32 v26, vcc, s42, v20
	v_pk_fma_f32 v[28:29], v[86:87], v[18:19], v[6:7] op_sel_hi:[1,0,1]
	s_nop 0
	v_addc_co_u32_e32 v27, vcc, 0, v21, vcc
	global_store_dwordx4 v[26:27], v[22:25], off
	v_pk_fma_f32 v[26:27], v[58:59], v[18:19], v[14:15] op_sel_hi:[1,0,1]
	s_nop 0
	v_pk_fma_f32 v[24:25], v[62:63], v[18:19], v[10:11] op_sel_hi:[1,0,1]
	v_mov_b32_e32 v22, 0
	v_mov_b32_e32 v23, 0
	v_cvt_pk_fp8_f32 v22, v24, v25
	v_cvt_pk_fp8_f32 v23, v26, v27
	v_pk_fma_f32 v[24:25], v[64:65], v[18:19], v[12:13] op_sel_hi:[1,0,1]
	v_pk_fma_f32 v[26:27], v[60:61], v[18:19], v[16:17] op_sel_hi:[1,0,1]
	v_cvt_pk_fp8_f32 v22, v24, v25 op_sel:[0,0,1]
	v_cvt_pk_fp8_f32 v23, v26, v27 op_sel:[0,0,1]
	v_pk_fma_f32 v[26:27], v[82:83], v[18:19], v[2:3] op_sel_hi:[1,0,1]
	v_mov_b32_e32 v24, 0
	v_mov_b32_e32 v25, 0
	v_cvt_pk_fp8_f32 v24, v26, v27
	v_cvt_pk_fp8_f32 v25, v28, v29
	v_pk_fma_f32 v[26:27], v[84:85], v[18:19], v[4:5] op_sel_hi:[1,0,1]
	v_pk_fma_f32 v[28:29], v[88:89], v[18:19], v[8:9] op_sel_hi:[1,0,1]
	v_cvt_pk_fp8_f32 v24, v26, v27 op_sel:[0,0,1]
	v_cvt_pk_fp8_f32 v25, v28, v29 op_sel:[0,0,1]
	v_add_co_u32_e32 v26, vcc, s45, v20
	v_pk_fma_f32 v[28:29], v[70:71], v[18:19], v[6:7] op_sel_hi:[1,0,1]
	s_nop 0
	v_addc_co_u32_e32 v27, vcc, 0, v21, vcc
	global_store_dwordx4 v[26:27], v[22:25], off
	v_pk_fma_f32 v[26:27], v[42:43], v[18:19], v[14:15] op_sel_hi:[1,0,1]
	v_pk_fma_f32 v[14:15], v[34:35], v[18:19], v[14:15] op_sel_hi:[1,0,1]
	v_pk_fma_f32 v[24:25], v[46:47], v[18:19], v[10:11] op_sel_hi:[1,0,1]
	v_mov_b32_e32 v22, 0
	v_mov_b32_e32 v23, 0
	v_cvt_pk_fp8_f32 v22, v24, v25
	v_cvt_pk_fp8_f32 v23, v26, v27
	v_pk_fma_f32 v[24:25], v[48:49], v[18:19], v[12:13] op_sel_hi:[1,0,1]
	v_pk_fma_f32 v[26:27], v[44:45], v[18:19], v[16:17] op_sel_hi:[1,0,1]
	v_cvt_pk_fp8_f32 v22, v24, v25 op_sel:[0,0,1]
	v_cvt_pk_fp8_f32 v23, v26, v27 op_sel:[0,0,1]
	v_pk_fma_f32 v[26:27], v[66:67], v[18:19], v[2:3] op_sel_hi:[1,0,1]
	v_mov_b32_e32 v24, 0
	v_mov_b32_e32 v25, 0
	v_cvt_pk_fp8_f32 v24, v26, v27
	v_cvt_pk_fp8_f32 v25, v28, v29
	v_pk_fma_f32 v[26:27], v[68:69], v[18:19], v[4:5] op_sel_hi:[1,0,1]
	v_pk_fma_f32 v[28:29], v[72:73], v[18:19], v[8:9] op_sel_hi:[1,0,1]
	v_cvt_pk_fp8_f32 v24, v26, v27 op_sel:[0,0,1]
	v_cvt_pk_fp8_f32 v25, v28, v29 op_sel:[0,0,1]
	v_add_co_u32_e32 v26, vcc, s46, v20
	v_pk_fma_f32 v[12:13], v[40:41], v[18:19], v[12:13] op_sel_hi:[1,0,1]
	s_nop 0
	v_addc_co_u32_e32 v27, vcc, 0, v21, vcc
	global_store_dwordx4 v[26:27], v[22:25], off
	v_pk_fma_f32 v[2:3], v[50:51], v[18:19], v[2:3] op_sel_hi:[1,0,1]
	v_pk_fma_f32 v[6:7], v[54:55], v[18:19], v[6:7] op_sel_hi:[1,0,1]
	v_pk_fma_f32 v[22:23], v[38:39], v[18:19], v[10:11] op_sel_hi:[1,0,1]
	v_mov_b32_e32 v10, 0
	v_cvt_pk_fp8_f32 v10, v22, v23
	v_mov_b32_e32 v11, 0
	v_cvt_pk_fp8_f32 v11, v14, v15
	v_pk_fma_f32 v[14:15], v[36:37], v[18:19], v[16:17] op_sel_hi:[1,0,1]
	v_cvt_pk_fp8_f32 v10, v12, v13 op_sel:[0,0,1]
	v_mov_b32_e32 v12, 0
	v_mov_b32_e32 v13, 0
	v_cvt_pk_fp8_f32 v12, v2, v3
	v_cvt_pk_fp8_f32 v13, v6, v7
	v_pk_fma_f32 v[2:3], v[52:53], v[18:19], v[4:5] op_sel_hi:[1,0,1]
	v_pk_fma_f32 v[4:5], v[56:57], v[18:19], v[8:9] op_sel_hi:[1,0,1]
	v_cvt_pk_fp8_f32 v11, v14, v15 op_sel:[0,0,1]
	v_cvt_pk_fp8_f32 v12, v2, v3 op_sel:[0,0,1]
	v_cvt_pk_fp8_f32 v13, v4, v5 op_sel:[0,0,1]
	v_add_co_u32_e32 v2, vcc, 0x58000, v20
	s_nop 1
	v_addc_co_u32_e32 v3, vcc, 0, v21, vcc
	s_andn2_b64 vcc, exec, s[22:23]
	s_mov_b64 s[22:23], -1
	global_store_dwordx4 v[2:3], v[10:13], off
	s_cbranch_vccnz .LBB0_1413
	s_andn2_b64 vcc, exec, s[6:7]
	s_cbranch_vccnz .LBB0_1412
	s_barrier
	s_branch .LBB0_1412
